# scores/state/retention-output GEMMs: single-use operand LDS-DMA pieces use the default cache policy instead of non-temporal (each 128-B line is touched by two DMA instructions)
# speedup vs baseline: 1.0163x; 1.0002x over previous
.LBB0_1208:
	s_cmp_lt_i32 s92, 6
	s_cselect_b64 s[0:1], -1, 0
	s_cmp_gt_i32 s93, 5
	s_cselect_b64 s[2:3], -1, 0
	s_and_b64 s[0:1], s[0:1], s[2:3]
	v_cndmask_b32_e64 v0, 0, 1, s[0:1]
	v_cmp_ne_u32_e64 s[4:5], 1, v0
	s_andn2_b64 vcc, exec, s[0:1]
	v_mbcnt_lo_u32_b32 v0, -1, 0
	v_mbcnt_hi_u32_b32 v0, -1, v0
	s_cbranch_vccnz .LBB0_1289
	s_load_dword s0, s[90:91], 0x100
	s_ashr_i32 s1, s94, 31
	v_mbcnt_lo_u32_b32 v0, -1, 0
	v_mbcnt_hi_u32_b32 v0, -1, v0
	s_mov_b32 s2, 4
	v_add_u32_e32 v1, s52, v0
	s_waitcnt lgkmcnt(0)
	s_ashr_i32 s0, s0, 31
	s_cmpk_gt_i32 s94, 0x1ff
	v_readfirstlane_b32 s6, v1
	s_mov_b32 s3, 4
	s_cbranch_scc1 .LBB0_1239
	v_ashrrev_i32_e32 v3, 31, v1
	v_lshrrev_b32_e32 v3, 26, v3
	v_lshlrev_b32_e32 v2, 4, v1
	v_add_u32_e32 v3, v1, v3
	v_bfe_i32 v1, v1, 27, 1
	v_lshrrev_b32_e32 v1, 22, v1
	v_add_u32_e32 v1, v2, v1
	v_and_b32_e32 v1, 0xfffffc00, v1
	v_sub_u32_e32 v1, v2, v1
	s_ashr_i32 s8, s94, 3
	s_waitcnt vmcnt(0)
	v_lshrrev_b32_e32 v4, 4, v1
	s_ashr_i32 s9, s8, 31
	s_lshl_b32 s7, s94, 8
	v_bitop3_b32 v1, v4, v1, 32 bitop3:0x6c
	s_and_b32 s67, s8, 3
	s_lshl_b64 s[8:9], s[8:9], 11
	s_and_b32 s7, s7, 0x700
	v_ashrrev_i32_e32 v5, 31, v1
	s_or_b32 s8, s8, s7
	v_ashrrev_i32_e32 v3, 6, v3
	v_lshrrev_b32_e32 v5, 26, v5
	s_mulk_i32 s9, 0x600
	s_mul_hi_u32 s10, s8, 0x600
	v_lshlrev_b32_e32 v4, 3, v3
	v_add_u32_e32 v5, v1, v5
	s_add_i32 s10, s10, s9
	s_mulk_i32 s8, 0x600
	v_and_b32_e32 v4, -16, v4
	v_ashrrev_i32_e32 v6, 6, v5
	v_add_u32_e32 v2, 0x2000, v2
	s_add_u32 s36, s24, s8
	v_add_u32_e32 v7, v6, v4
	v_and_b32_e32 v4, 0xc0, v5
	v_ashrrev_i32_e32 v5, 31, v2
	s_addc_u32 s37, s25, s10
	v_lshrrev_b32_e32 v5, 22, v5
	s_add_u32 s38, s36, 0x200
	v_add_u32_e32 v5, v2, v5
	s_addc_u32 s39, s37, 0
	v_ashrrev_i32_e32 v5, 10, v5
	s_add_u32 s46, s26, 0x63800000
	v_mul_i32_i24_e32 v8, 0x400, v5
	s_addc_u32 s47, s27, 0
	s_lshl_b32 s8, s94, 6
	v_sub_u32_e32 v2, v2, v8
	s_and_b32 s8, s8, 0xfffff800
	v_lshrrev_b32_e32 v8, 4, v2
	s_or_b32 s8, s8, s7
	v_bitop3_b32 v2, v8, v2, 32 bitop3:0x6c
	s_ashr_i32 s9, s8, 31
	v_ashrrev_i32_e32 v9, 31, v2
	s_lshl_b32 s7, s67, 9
	s_lshl_b64 s[8:9], s[8:9], 11
	v_lshrrev_b32_e32 v9, 26, v9
	s_add_u32 s8, s46, s8
	v_add_u32_e32 v9, v2, v9
	s_addc_u32 s9, s47, s9
	v_ashrrev_i32_e32 v10, 6, v9
	v_and_b32_e32 v9, 0xc0, v9
	s_add_u32 s44, s8, s7
	v_sub_u32_e32 v1, v1, v4
	v_mov_b32_e32 v4, 1
	v_sub_u32_e32 v2, v2, v9
	s_addc_u32 s45, s9, 0
	v_lshlrev_b32_e32 v8, 3, v5
	v_ashrrev_i16_sdwa v2, v4, sext(v2) dst_sel:DWORD dst_unused:UNUSED_PAD src0_sel:DWORD src1_sel:BYTE_0
	s_add_u32 s42, s44, 0x40000
	v_ashrrev_i16_sdwa v1, v4, sext(v1) dst_sel:DWORD dst_unused:UNUSED_PAD src0_sel:DWORD src1_sel:BYTE_0
	v_and_b32_e32 v8, -16, v8
	v_bfe_i32 v4, v2, 0, 16
	v_lshlrev_b32_e32 v2, 1, v7
	v_lshrrev_b32_e32 v9, 2, v7
	v_and_b32_e32 v6, 3, v6
	s_mov_b32 s8, 0x1fffe0
	s_addc_u32 s43, s45, 0
	v_add_u32_e32 v8, v10, v8
	v_and_b32_e32 v2, 24, v2
	v_and_b32_e32 v9, 4, v9
	v_and_or_b32 v6, v7, s8, v6
	s_add_u32 s40, s36, 0x30200
	v_lshlrev_b32_e32 v3, 5, v3
	v_lshlrev_b32_e32 v5, 5, v5
	v_or3_b32 v6, v6, v9, v2
	v_lshlrev_b32_e32 v2, 1, v8
	v_lshrrev_b32_e32 v9, 2, v8
	v_and_b32_e32 v10, 3, v10
	s_addc_u32 s41, s37, 0
	s_ashr_i32 s7, s6, 6
	v_and_b32_e32 v3, 32, v3
	v_bfe_i32 v1, v1, 0, 16
	v_and_b32_e32 v5, 32, v5
	v_and_b32_e32 v2, 24, v2
	v_and_b32_e32 v9, 4, v9
	v_and_or_b32 v10, v8, s8, v10
	s_movk_i32 s33, 0x600
	v_or3_b32 v9, v10, v9, v2
	v_add_lshl_u32 v2, v3, v1, 1
	v_add_lshl_u32 v4, v5, v4, 1
	s_lshl_b32 s48, s7, 10
	v_lshl_add_u32 v138, v6, 11, v2
	v_lshl_add_u32 v139, v9, 11, v4
	v_mad_u64_u32 v[128:129], s[8:9], v7, s33, v[2:3]
	v_mad_u64_u32 v[130:131], s[8:9], v8, s33, v[4:5]
	s_add_i32 s49, s48, 0
	v_mov_b32_e32 v1, v139
	s_mov_b64 s[8:9], s[44:45]
	v_mov_b32_e32 v2, v138
	s_add_i32 m0, s49, 0x10000
	s_add_i32 s50, s49, 0x2000
	global_load_lds_dwordx4 v2, s[8:9]
	s_add_i32 m0, s49, 0x12000
	v_mov_b32_e32 v2, v138
	global_load_lds_dwordx4 v1, s[8:9]
	v_mov_b32_e32 v1, v139
	s_mov_b64 s[8:9], s[42:43]
	s_add_i32 m0, s49, 0x14000
	s_add_i32 s51, s49, 0x4000
	global_load_lds_dwordx4 v2, s[8:9]
	s_add_i32 m0, s49, 0x16000
	v_mov_b32_e32 v2, v130
	global_load_lds_dwordx4 v1, s[8:9]
	v_mov_b32_e32 v1, v128
	s_mov_b64 s[8:9], s[38:39]
	s_mov_b32 m0, s49
	s_add_i32 s52, s49, 0x6000
	global_load_lds_dwordx4 v1, s[8:9]
	s_mov_b32 m0, s50
	v_mov_b32_e32 v1, v130
	global_load_lds_dwordx4 v2, s[8:9]
	v_mov_b32_e32 v2, v128
	s_mov_b64 s[8:9], s[40:41]
	s_mov_b32 m0, s51
	s_ashr_i32 s10, s6, 8
	global_load_lds_dwordx4 v2, s[8:9]
	s_mov_b32 m0, s52
	s_cmp_eq_u32 s10, 1
	global_load_lds_dwordx4 v1, s[8:9]
	s_mov_b32 s53, 0
	s_mov_b32 s54, 0x12000
	s_cselect_b64 s[8:9], -1, 0
	s_cmp_lg_u32 s10, 1
	s_movk_i32 s55, 0x6000
	s_cbranch_scc1 .LBB0_1212
	s_barrier
.LBB0_1212:
	s_add_u32 s12, s44, 0x80
	s_addc_u32 s13, s45, 0
	s_add_u32 s14, s36, 0x280
	s_addc_u32 s15, s37, 0
	s_add_u32 s16, s44, 0x40080
	s_addc_u32 s17, s45, 0
	v_mov_b32_e32 v1, v139
	v_mov_b32_e32 v2, v138
	s_add_i32 m0, s49, 0x18000
	s_waitcnt vmcnt(2)
	s_barrier
	s_add_i32 s56, s49, 0x8000
	global_load_lds_dwordx4 v2, s[12:13]
	s_add_i32 m0, s49, 0x1a000
	v_mov_b32_e32 v2, v130
	global_load_lds_dwordx4 v1, s[12:13]
	v_mov_b32_e32 v1, v128
	s_mov_b32 m0, s56
	s_add_i32 s57, s49, 0xa000
	s_lshl_b32 s7, s7, 5
	global_load_lds_dwordx4 v1, s[14:15]
	s_mov_b32 m0, s57
	v_mov_b32_e32 v1, v139
	global_load_lds_dwordx4 v2, s[14:15]
	v_mov_b32_e32 v2, v138
	s_add_i32 m0, s49, 0x1c000
	s_and_b32 s7, s7, 0x60
	global_load_lds_dwordx4 v2, s[16:17]
	s_add_i32 m0, s49, 0x1e000
	v_lshrrev_b32_e32 v2, 1, v0
	global_load_lds_dwordx4 v1, s[16:17]
	v_and_b32_e32 v2, 24, v2
	v_and_b32_e32 v1, 15, v0
	v_lshlrev_b32_e32 v3, 1, v2
	v_lshlrev_b32_e32 v0, 2, v0
	v_lshl_or_b32 v129, s10, 6, v1
	v_lshl_or_b32 v1, v1, 6, v3
	s_lshl_b32 s10, s10, 13
	v_and_b32_e32 v0, 32, v0
	v_bitop3_b32 v3, v1, s10, v0 bitop3:0xde
	s_lshl_b32 s10, s7, 7
	s_cmp_gt_i32 s3, 0
	v_bitop3_b32 v131, v1, s10, v0 bitop3:0xde
	s_cselect_b64 s[10:11], -1, 0
	s_add_i32 s58, s3, -2
	s_waitcnt vmcnt(6)
	s_cmpk_lt_u32 s6, 0x100
	s_cselect_b64 s[12:13], -1, 0
	s_add_i32 s59, 0, 0x10000
	s_add_i32 s60, 0, 0x14000
	v_or_b32_e32 v140, s7, v2
	v_add_u32_e32 v141, s59, v131
	s_mov_b32 s61, 0xc000
	v_add_u32_e32 v142, s60, v131
	v_add_u32_e32 v143, 0, v3
	s_mov_b32 s62, 0x30000
	s_mov_b32 s63, 0x36000
	s_mov_b32 s64, 0x3c000
	s_mov_b32 s65, 0x42000
	v_mov_b64_e32 v[132:133], 0x1ff
	v_mov_b32_e32 v144, 0xbbb906ce
	v_mov_b32_e32 v145, 0xbc3963d9
	s_barrier
	s_branch .LBB0_1215

.LBB0_1223:
	ds_read_b128 v[134:137], v141
	ds_read_b128 v[146:149], v141 offset:1024
	ds_read_b128 v[150:153], v141 offset:2048
	ds_read_b128 v[154:157], v141 offset:3072
	ds_read_b128 v[158:161], v142
	ds_read_b128 v[162:165], v142 offset:1024
	ds_read_b128 v[166:169], v142 offset:2048
	ds_read_b128 v[170:173], v142 offset:3072
	s_add_i32 s76, s38, 2
	s_add_u32 s44, s74, 0xffffff80
	s_addc_u32 s45, s75, -1
	s_add_i32 m0, s49, 0xc000
	s_add_i32 s77, s49, 0xe000
	s_cmp_eq_u32 s58, s38
	s_cselect_b32 s38, s34, s72
	s_cselect_b32 s39, s35, s73
	s_cselect_b32 s41, s31, s69
	s_cselect_b32 s40, s30, s68
	s_cselect_b32 s43, s23, s75
	s_cselect_b32 s42, s22, s74
	v_mov_b32_e32 v206, v128
	v_mov_b32_e32 v207, v130
	ds_read_b128 v[174:177], v143
	ds_read_b128 v[178:181], v143 offset:1024
	ds_read_b128 v[182:185], v143 offset:2048
	ds_read_b128 v[186:189], v143 offset:3072
	ds_read_b128 v[190:193], v143 offset:4096
	ds_read_b128 v[194:197], v143 offset:5120
	ds_read_b128 v[198:201], v143 offset:6144
	ds_read_b128 v[202:205], v143 offset:7168
	s_nop 0
	global_load_lds_dwordx4 v206, s[44:45]
	s_mov_b32 m0, s77
	s_nop 0
	global_load_lds_dwordx4 v207, s[44:45]
	s_waitcnt vmcnt(8)
	s_waitcnt lgkmcnt(0)
	s_barrier
	s_setprio 1
	s_waitcnt lgkmcnt(0)
	v_mfma_f32_16x16x32_bf16 v[124:127], v[134:137], v[174:177], v[124:127]
	v_mfma_f32_16x16x32_bf16 v[120:123], v[150:153], v[174:177], v[120:123]
	v_mfma_f32_16x16x32_bf16 v[108:111], v[134:137], v[182:185], v[108:111]
	v_mfma_f32_16x16x32_bf16 v[104:107], v[150:153], v[182:185], v[104:107]
	v_mfma_f32_16x16x32_bf16 v[92:95], v[134:137], v[190:193], v[92:95]
	v_mfma_f32_16x16x32_bf16 v[88:91], v[150:153], v[190:193], v[88:91]
	v_mfma_f32_16x16x32_bf16 v[76:79], v[134:137], v[198:201], v[76:79]
	v_mfma_f32_16x16x32_bf16 v[72:75], v[150:153], v[198:201], v[72:75]
	v_mfma_f32_16x16x32_bf16 v[124:127], v[146:149], v[178:181], v[124:127]
	v_mfma_f32_16x16x32_bf16 v[120:123], v[154:157], v[178:181], v[120:123]
	v_mfma_f32_16x16x32_bf16 v[108:111], v[146:149], v[186:189], v[108:111]
	v_mfma_f32_16x16x32_bf16 v[104:107], v[154:157], v[186:189], v[104:107]
	v_mfma_f32_16x16x32_bf16 v[92:95], v[146:149], v[194:197], v[92:95]
	v_mfma_f32_16x16x32_bf16 v[88:91], v[154:157], v[194:197], v[88:91]
	v_mfma_f32_16x16x32_bf16 v[76:79], v[146:149], v[202:205], v[76:79]
	v_mfma_f32_16x16x32_bf16 v[72:75], v[154:157], v[202:205], v[72:75]
	s_setprio 0
	s_setprio 1
	v_mfma_f32_16x16x32_bf16 v[116:119], v[158:161], v[174:177], v[116:119]
	v_mfma_f32_16x16x32_bf16 v[112:115], v[166:169], v[174:177], v[112:115]
	v_mfma_f32_16x16x32_bf16 v[100:103], v[158:161], v[182:185], v[100:103]
	v_mfma_f32_16x16x32_bf16 v[96:99], v[166:169], v[182:185], v[96:99]
	v_mfma_f32_16x16x32_bf16 v[84:87], v[158:161], v[190:193], v[84:87]
	v_mfma_f32_16x16x32_bf16 v[80:83], v[166:169], v[190:193], v[80:83]
	v_mfma_f32_16x16x32_bf16 v[68:71], v[158:161], v[198:201], v[68:71]
	v_mfma_f32_16x16x32_bf16 v[64:67], v[166:169], v[198:201], v[64:67]
	v_mfma_f32_16x16x32_bf16 v[116:119], v[162:165], v[178:181], v[116:119]
	v_mfma_f32_16x16x32_bf16 v[112:115], v[170:173], v[178:181], v[112:115]
	v_mfma_f32_16x16x32_bf16 v[100:103], v[162:165], v[186:189], v[100:103]
	v_mfma_f32_16x16x32_bf16 v[96:99], v[170:173], v[186:189], v[96:99]
	v_mfma_f32_16x16x32_bf16 v[84:87], v[162:165], v[194:197], v[84:87]
	v_mfma_f32_16x16x32_bf16 v[80:83], v[170:173], v[194:197], v[80:83]
	v_mfma_f32_16x16x32_bf16 v[68:71], v[162:165], v[202:205], v[68:71]
	v_mfma_f32_16x16x32_bf16 v[64:67], v[170:173], v[202:205], v[64:67]
	s_setprio 0
	s_barrier
	s_cselect_b32 s45, s29, s71
	s_cselect_b32 s44, s28, s70
	s_add_i32 s77, s59, s48
	v_mov_b32_e32 v206, v139
	v_mov_b32_e32 v207, v138
	s_mov_b64 s[78:79], s[40:41]
	s_mov_b32 m0, s77
	ds_read_b128 v[174:177], v143 offset:16384
	ds_read_b128 v[178:181], v143 offset:17408
	ds_read_b128 v[182:185], v143 offset:18432
	ds_read_b128 v[186:189], v143 offset:19456
	ds_read_b128 v[190:193], v143 offset:20480
	ds_read_b128 v[194:197], v143 offset:21504
	ds_read_b128 v[198:201], v143 offset:22528
	ds_read_b128 v[202:205], v143 offset:23552
	s_nop 0
	global_load_lds_dwordx4 v207, s[78:79]
	s_add_i32 m0, s77, 0x2000
	s_add_i32 s77, s60, s48
	global_load_lds_dwordx4 v206, s[78:79]
	v_mov_b32_e32 v206, v139
	s_mov_b64 s[78:79], s[44:45]
	v_mov_b32_e32 v207, v138
	s_mov_b32 m0, s77
	s_nop 0
	global_load_lds_dwordx4 v207, s[78:79]
	s_add_i32 m0, s77, 0x2000
	v_mov_b32_e32 v207, v130
	global_load_lds_dwordx4 v206, s[78:79]
	v_mov_b32_e32 v206, v128
	s_mov_b64 s[78:79], s[38:39]
	s_mov_b32 m0, s49
	s_nop 0
	global_load_lds_dwordx4 v206, s[78:79]
	s_mov_b32 m0, s50
	s_nop 0
	global_load_lds_dwordx4 v207, s[78:79]
	s_waitcnt vmcnt(8)
	s_waitcnt lgkmcnt(0)
	s_barrier
	s_setprio 1
	s_waitcnt lgkmcnt(0)
	v_mfma_f32_16x16x32_bf16 v[60:63], v[134:137], v[174:177], v[60:63]
	v_mfma_f32_16x16x32_bf16 v[56:59], v[150:153], v[174:177], v[56:59]
	v_mfma_f32_16x16x32_bf16 v[44:47], v[134:137], v[182:185], v[44:47]
	v_mfma_f32_16x16x32_bf16 v[40:43], v[150:153], v[182:185], v[40:43]
	v_mfma_f32_16x16x32_bf16 v[28:31], v[134:137], v[190:193], v[28:31]
	v_mfma_f32_16x16x32_bf16 v[24:27], v[150:153], v[190:193], v[24:27]
	v_mfma_f32_16x16x32_bf16 v[12:15], v[134:137], v[198:201], v[12:15]
	v_mfma_f32_16x16x32_bf16 v[8:11], v[150:153], v[198:201], v[8:11]
	v_mfma_f32_16x16x32_bf16 v[60:63], v[146:149], v[178:181], v[60:63]
	v_mfma_f32_16x16x32_bf16 v[56:59], v[154:157], v[178:181], v[56:59]
	v_mfma_f32_16x16x32_bf16 v[44:47], v[146:149], v[186:189], v[44:47]
	v_mfma_f32_16x16x32_bf16 v[40:43], v[154:157], v[186:189], v[40:43]
	v_mfma_f32_16x16x32_bf16 v[28:31], v[146:149], v[194:197], v[28:31]
	v_mfma_f32_16x16x32_bf16 v[24:27], v[154:157], v[194:197], v[24:27]
	v_mfma_f32_16x16x32_bf16 v[12:15], v[146:149], v[202:205], v[12:15]
	v_mfma_f32_16x16x32_bf16 v[8:11], v[154:157], v[202:205], v[8:11]
	s_setprio 0
	s_setprio 1
	v_mfma_f32_16x16x32_bf16 v[52:55], v[158:161], v[174:177], v[52:55]
	v_mfma_f32_16x16x32_bf16 v[48:51], v[166:169], v[174:177], v[48:51]
	v_mfma_f32_16x16x32_bf16 v[36:39], v[158:161], v[182:185], v[36:39]
	v_mfma_f32_16x16x32_bf16 v[32:35], v[166:169], v[182:185], v[32:35]
	v_mfma_f32_16x16x32_bf16 v[20:23], v[158:161], v[190:193], v[20:23]
	v_mfma_f32_16x16x32_bf16 v[16:19], v[166:169], v[190:193], v[16:19]
	v_mfma_f32_16x16x32_bf16 v[4:7], v[158:161], v[198:201], v[4:7]
	v_mfma_f32_16x16x32_bf16 v[0:3], v[166:169], v[198:201], v[0:3]
	v_mfma_f32_16x16x32_bf16 v[52:55], v[162:165], v[178:181], v[52:55]
	v_mfma_f32_16x16x32_bf16 v[48:51], v[170:173], v[178:181], v[48:51]
	v_mfma_f32_16x16x32_bf16 v[36:39], v[162:165], v[186:189], v[36:39]
	v_mfma_f32_16x16x32_bf16 v[32:35], v[170:173], v[186:189], v[32:35]
	v_mfma_f32_16x16x32_bf16 v[20:23], v[162:165], v[194:197], v[20:23]
	v_mfma_f32_16x16x32_bf16 v[16:19], v[170:173], v[194:197], v[16:19]
	v_mfma_f32_16x16x32_bf16 v[4:7], v[162:165], v[202:205], v[4:7]
	v_mfma_f32_16x16x32_bf16 v[0:3], v[170:173], v[202:205], v[0:3]
	s_setprio 0
	s_barrier
	s_add_i32 s77, 0, 0x18000
	s_add_i32 s78, 0, 0x1c000
	v_add_u32_e32 v154, s77, v131
	v_add_u32_e32 v170, s78, v131
	ds_read_b128 v[134:137], v154
	ds_read_b128 v[146:149], v154 offset:1024
	ds_read_b128 v[150:153], v154 offset:2048
	ds_read_b128 v[154:157], v154 offset:3072
	ds_read_b128 v[158:161], v170
	ds_read_b128 v[162:165], v170 offset:1024
	ds_read_b128 v[166:169], v170 offset:2048
	ds_read_b128 v[170:173], v170 offset:3072
	v_mov_b32_e32 v206, v128
	v_mov_b32_e32 v207, v130
	s_mov_b32 m0, s51
	ds_read_b128 v[174:177], v143 offset:32768
	ds_read_b128 v[178:181], v143 offset:33792
	ds_read_b128 v[182:185], v143 offset:34816
	ds_read_b128 v[186:189], v143 offset:35840
	ds_read_b128 v[190:193], v143 offset:36864
	ds_read_b128 v[194:197], v143 offset:37888
	ds_read_b128 v[198:201], v143 offset:38912
	ds_read_b128 v[202:205], v143 offset:39936
	s_nop 0
	global_load_lds_dwordx4 v206, s[42:43]
	s_mov_b32 m0, s52
	s_nop 0
	global_load_lds_dwordx4 v207, s[42:43]
	s_waitcnt vmcnt(8)
	s_waitcnt lgkmcnt(0)
	s_barrier
	s_setprio 1
	s_waitcnt lgkmcnt(0)
	v_mfma_f32_16x16x32_bf16 v[124:127], v[134:137], v[174:177], v[124:127]
	v_mfma_f32_16x16x32_bf16 v[120:123], v[150:153], v[174:177], v[120:123]
	v_mfma_f32_16x16x32_bf16 v[108:111], v[134:137], v[182:185], v[108:111]
	v_mfma_f32_16x16x32_bf16 v[104:107], v[150:153], v[182:185], v[104:107]
	v_mfma_f32_16x16x32_bf16 v[92:95], v[134:137], v[190:193], v[92:95]
	v_mfma_f32_16x16x32_bf16 v[88:91], v[150:153], v[190:193], v[88:91]
	v_mfma_f32_16x16x32_bf16 v[76:79], v[134:137], v[198:201], v[76:79]
	v_mfma_f32_16x16x32_bf16 v[72:75], v[150:153], v[198:201], v[72:75]
	v_mfma_f32_16x16x32_bf16 v[124:127], v[146:149], v[178:181], v[124:127]
	v_mfma_f32_16x16x32_bf16 v[120:123], v[154:157], v[178:181], v[120:123]
	v_mfma_f32_16x16x32_bf16 v[108:111], v[146:149], v[186:189], v[108:111]
	v_mfma_f32_16x16x32_bf16 v[104:107], v[154:157], v[186:189], v[104:107]
	v_mfma_f32_16x16x32_bf16 v[92:95], v[146:149], v[194:197], v[92:95]
	v_mfma_f32_16x16x32_bf16 v[88:91], v[154:157], v[194:197], v[88:91]
	v_mfma_f32_16x16x32_bf16 v[76:79], v[146:149], v[202:205], v[76:79]
	v_mfma_f32_16x16x32_bf16 v[72:75], v[154:157], v[202:205], v[72:75]
	s_setprio 0
	s_setprio 1
	v_mfma_f32_16x16x32_bf16 v[116:119], v[158:161], v[174:177], v[116:119]
	v_mfma_f32_16x16x32_bf16 v[112:115], v[166:169], v[174:177], v[112:115]
	v_mfma_f32_16x16x32_bf16 v[100:103], v[158:161], v[182:185], v[100:103]
	v_mfma_f32_16x16x32_bf16 v[96:99], v[166:169], v[182:185], v[96:99]
	v_mfma_f32_16x16x32_bf16 v[84:87], v[158:161], v[190:193], v[84:87]
	v_mfma_f32_16x16x32_bf16 v[80:83], v[166:169], v[190:193], v[80:83]
	v_mfma_f32_16x16x32_bf16 v[68:71], v[158:161], v[198:201], v[68:71]
	v_mfma_f32_16x16x32_bf16 v[64:67], v[166:169], v[198:201], v[64:67]
	v_mfma_f32_16x16x32_bf16 v[116:119], v[162:165], v[178:181], v[116:119]
	v_mfma_f32_16x16x32_bf16 v[112:115], v[170:173], v[178:181], v[112:115]
	v_mfma_f32_16x16x32_bf16 v[100:103], v[162:165], v[186:189], v[100:103]
	v_mfma_f32_16x16x32_bf16 v[96:99], v[170:173], v[186:189], v[96:99]
	v_mfma_f32_16x16x32_bf16 v[84:87], v[162:165], v[194:197], v[84:87]
	v_mfma_f32_16x16x32_bf16 v[80:83], v[170:173], v[194:197], v[80:83]
	v_mfma_f32_16x16x32_bf16 v[68:71], v[162:165], v[202:205], v[68:71]
	v_mfma_f32_16x16x32_bf16 v[64:67], v[170:173], v[202:205], v[64:67]
	s_setprio 0
	s_barrier
	s_add_u32 s40, s40, 0x80
	s_addc_u32 s41, s41, 0
	s_add_i32 s42, s77, s48
	v_mov_b32_e32 v206, v139
	v_mov_b32_e32 v207, v138
	s_mov_b32 m0, s42
	ds_read_b128 v[174:177], v143 offset:49152
	ds_read_b128 v[178:181], v143 offset:50176
	ds_read_b128 v[182:185], v143 offset:51200
	ds_read_b128 v[186:189], v143 offset:52224
	ds_read_b128 v[190:193], v143 offset:53248
	ds_read_b128 v[194:197], v143 offset:54272
	ds_read_b128 v[198:201], v143 offset:55296
	ds_read_b128 v[202:205], v143 offset:56320
	s_nop 0
	global_load_lds_dwordx4 v207, s[40:41]
	s_add_i32 m0, s42, 0x2000
	v_mov_b32_e32 v207, v138
	global_load_lds_dwordx4 v206, s[40:41]
	s_add_u32 s40, s44, 0x80
	s_addc_u32 s41, s45, 0
	s_add_i32 s42, s78, s48
	v_mov_b32_e32 v206, v139
	s_mov_b32 m0, s42
	s_nop 0
	global_load_lds_dwordx4 v207, s[40:41]
	s_add_i32 m0, s42, 0x2000
	s_add_u32 s38, s38, 0x80
	global_load_lds_dwordx4 v206, s[40:41]
	s_addc_u32 s39, s39, 0
	v_mov_b32_e32 v206, v128
	v_mov_b32_e32 v207, v130
	s_mov_b32 m0, s56
	s_nop 0
	global_load_lds_dwordx4 v206, s[38:39]
	s_mov_b32 m0, s57
	s_nop 0
	global_load_lds_dwordx4 v207, s[38:39]
	s_waitcnt vmcnt(8)
	s_waitcnt lgkmcnt(0)
	s_barrier
	s_setprio 1
	s_waitcnt lgkmcnt(0)
	v_mfma_f32_16x16x32_bf16 v[60:63], v[134:137], v[174:177], v[60:63]
	v_mfma_f32_16x16x32_bf16 v[56:59], v[150:153], v[174:177], v[56:59]
	v_mfma_f32_16x16x32_bf16 v[44:47], v[134:137], v[182:185], v[44:47]
	v_mfma_f32_16x16x32_bf16 v[40:43], v[150:153], v[182:185], v[40:43]
	v_mfma_f32_16x16x32_bf16 v[28:31], v[134:137], v[190:193], v[28:31]
	v_mfma_f32_16x16x32_bf16 v[24:27], v[150:153], v[190:193], v[24:27]
	v_mfma_f32_16x16x32_bf16 v[12:15], v[134:137], v[198:201], v[12:15]
	v_mfma_f32_16x16x32_bf16 v[8:11], v[150:153], v[198:201], v[8:11]
	v_mfma_f32_16x16x32_bf16 v[60:63], v[146:149], v[178:181], v[60:63]
	v_mfma_f32_16x16x32_bf16 v[56:59], v[154:157], v[178:181], v[56:59]
	v_mfma_f32_16x16x32_bf16 v[44:47], v[146:149], v[186:189], v[44:47]
	v_mfma_f32_16x16x32_bf16 v[40:43], v[154:157], v[186:189], v[40:43]
	v_mfma_f32_16x16x32_bf16 v[28:31], v[146:149], v[194:197], v[28:31]
	v_mfma_f32_16x16x32_bf16 v[24:27], v[154:157], v[194:197], v[24:27]
	v_mfma_f32_16x16x32_bf16 v[12:15], v[146:149], v[202:205], v[12:15]
	v_mfma_f32_16x16x32_bf16 v[8:11], v[154:157], v[202:205], v[8:11]
	s_setprio 0
	s_setprio 1
	v_mfma_f32_16x16x32_bf16 v[52:55], v[158:161], v[174:177], v[52:55]
	v_mfma_f32_16x16x32_bf16 v[48:51], v[166:169], v[174:177], v[48:51]
	v_mfma_f32_16x16x32_bf16 v[36:39], v[158:161], v[182:185], v[36:39]
	v_mfma_f32_16x16x32_bf16 v[32:35], v[166:169], v[182:185], v[32:35]
	v_mfma_f32_16x16x32_bf16 v[20:23], v[158:161], v[190:193], v[20:23]
	v_mfma_f32_16x16x32_bf16 v[16:19], v[166:169], v[190:193], v[16:19]
	v_mfma_f32_16x16x32_bf16 v[4:7], v[158:161], v[198:201], v[4:7]
	v_mfma_f32_16x16x32_bf16 v[0:3], v[166:169], v[198:201], v[0:3]
	v_mfma_f32_16x16x32_bf16 v[52:55], v[162:165], v[178:181], v[52:55]
	v_mfma_f32_16x16x32_bf16 v[48:51], v[170:173], v[178:181], v[48:51]
	v_mfma_f32_16x16x32_bf16 v[36:39], v[162:165], v[186:189], v[36:39]
	v_mfma_f32_16x16x32_bf16 v[32:35], v[170:173], v[186:189], v[32:35]
	v_mfma_f32_16x16x32_bf16 v[20:23], v[162:165], v[194:197], v[20:23]
	v_mfma_f32_16x16x32_bf16 v[16:19], v[170:173], v[194:197], v[16:19]
	v_mfma_f32_16x16x32_bf16 v[4:7], v[162:165], v[202:205], v[4:7]
	v_mfma_f32_16x16x32_bf16 v[0:3], v[170:173], v[202:205], v[0:3]
	s_setprio 0
	s_barrier
	s_add_u32 s68, s68, 0x100
	s_addc_u32 s69, s69, 0
	s_add_u32 s70, s70, 0x100
	s_addc_u32 s71, s71, 0
	s_add_u32 s72, s72, 0x100
	s_addc_u32 s73, s73, 0
	s_add_u32 s74, s74, 0x100
	s_addc_u32 s75, s75, 0
	s_cmp_ge_i32 s76, s3
	s_mov_b32 s38, s76
	s_cbranch_scc0 .LBB0_1223
	s_and_b64 vcc, exec, s[12:13]
	s_cbranch_vccz .LBB0_1226

.LBB0_1239:
	v_mbcnt_lo_u32_b32 v0, -1, 0
	v_mbcnt_hi_u32_b32 v0, -1, v0
	s_cmpk_gt_i32 s94, 0x47f
	v_add_u32_e32 v1, s52, v0
	s_nop 0
	v_readfirstlane_b32 s6, v1
	s_cbranch_scc1 .LBB0_1260
	s_mul_hi_i32 s8, s94, 0x38e38e39
	s_lshr_b32 s9, s8, 31
	s_ashr_i32 s11, s8, 2
	s_add_i32 s11, s11, s9
	v_ashrrev_i32_e32 v3, 31, v1
	s_mul_i32 s8, s11, 18
	s_ashr_i32 s10, s6, 6
	v_lshrrev_b32_e32 v3, 26, v3
	s_sub_i32 s9, s94, s8
	s_ashr_i32 s7, s6, 8
	v_lshlrev_b32_e32 v2, 4, v1
	v_add_u32_e32 v3, v1, v3
	v_bfe_i32 v1, v1, 27, 1
	s_lshl_b32 s33, s10, 10
	s_ashr_i32 s12, s9, 1
	s_and_b32 s13, s9, 1
	s_ashr_i32 s8, s11, 2
	v_lshrrev_b32_e32 v1, 22, v1
	s_cmp_lt_u32 s9, 2
	v_add_u32_e32 v1, v2, v1
	s_cselect_b64 s[14:15], -1, 0
	s_lshl_b32 s9, s11, 3
	s_add_i32 s18, s12, -1
	v_and_b32_e32 v1, 0xfffffc00, v1
	s_add_i32 s9, s18, s9
	v_sub_u32_e32 v1, v2, v1
	s_and_b64 s[16:17], s[14:15], exec
	s_mov_b32 s46, 0x62000000
	s_waitcnt vmcnt(0)
	v_lshrrev_b32_e32 v4, 4, v1
	s_cselect_b32 s16, s46, 0x56000000
	v_bitop3_b32 v1, v4, v1, 32 bitop3:0x6c
	s_cselect_b32 s9, s11, s9
	s_add_u32 s16, s26, s16
	v_ashrrev_i32_e32 v5, 31, v1
	s_addc_u32 s17, s27, 0
	s_mul_hi_i32 s19, s9, 0x60000
	s_mul_i32 s9, s9, 0x60000
	v_ashrrev_i32_e32 v3, 6, v3
	v_lshrrev_b32_e32 v5, 26, v5
	s_add_u32 s38, s16, s9
	v_lshlrev_b32_e32 v4, 3, v3
	v_add_u32_e32 v5, v1, v5
	s_addc_u32 s39, s17, s19
	s_ashr_i32 s9, s8, 31
	v_and_b32_e32 v4, -16, v4
	v_ashrrev_i32_e32 v6, 6, v5
	v_add_u32_e32 v2, 0x2000, v2
	s_lshl_b64 s[16:17], s[8:9], 11
	v_add_u32_e32 v7, v6, v4
	v_and_b32_e32 v4, 0xc0, v5
	v_ashrrev_i32_e32 v5, 31, v2
	s_and_b64 s[14:15], s[14:15], exec
	v_lshrrev_b32_e32 v5, 22, v5
	s_cselect_b32 s8, s8, s18
	v_add_u32_e32 v5, v2, v5
	s_cselect_b32 s15, 0, s17
	s_cselect_b32 s14, 0x8000, s16
	s_ashr_i32 s9, s8, 31
	v_ashrrev_i32_e32 v5, 10, v5
	s_cmp_eq_u32 s13, 0
	s_mov_b32 s47, 0x67800000
	v_mul_i32_i24_e32 v8, 0x400, v5
	s_cselect_b32 s16, s47, 0x6c000000
	v_sub_u32_e32 v2, v2, v8
	s_add_u32 s16, s26, s16
	v_lshrrev_b32_e32 v8, 4, v2
	s_addc_u32 s17, s27, 0
	s_lshl_b32 s18, s11, 8
	v_bitop3_b32 v2, v8, v2, 32 bitop3:0x6c
	s_and_b32 s18, s18, 0x300
	v_ashrrev_i32_e32 v9, 31, v2
	s_mul_i32 s18, s18, 0x9000
	v_lshrrev_b32_e32 v9, 26, v9
	s_add_u32 s14, s14, s18
	v_add_u32_e32 v9, v2, v9
	s_addc_u32 s15, s15, 0
	v_ashrrev_i32_e32 v10, 6, v9
	v_and_b32_e32 v9, 0xc0, v9
	s_lshl_b64 s[8:9], s[8:9], 9
	s_lshl_b64 s[14:15], s[14:15], 1
	v_sub_u32_e32 v1, v1, v4
	v_mov_b32_e32 v4, 1
	v_sub_u32_e32 v2, v2, v9
	s_add_u32 s8, s16, s8
	v_lshlrev_b32_e32 v8, 3, v5
	v_ashrrev_i16_sdwa v2, v4, sext(v2) dst_sel:DWORD dst_unused:UNUSED_PAD src0_sel:DWORD src1_sel:BYTE_0
	s_addc_u32 s9, s17, s9
	v_ashrrev_i16_sdwa v1, v4, sext(v1) dst_sel:DWORD dst_unused:UNUSED_PAD src0_sel:DWORD src1_sel:BYTE_0
	v_and_b32_e32 v8, -16, v8
	v_bfe_i32 v4, v2, 0, 16
	v_lshlrev_b32_e32 v2, 1, v7
	v_lshrrev_b32_e32 v9, 2, v7
	v_and_b32_e32 v6, 3, v6
	s_mov_b32 s3, 0x7ffe0
	s_add_u32 s44, s8, s14
	v_add_u32_e32 v8, v10, v8
	v_and_b32_e32 v2, 24, v2
	v_and_b32_e32 v9, 4, v9
	v_and_or_b32 v6, v7, s3, v6
	s_addc_u32 s45, s9, s15
	v_lshlrev_b32_e32 v3, 5, v3
	v_lshlrev_b32_e32 v5, 5, v5
	v_or3_b32 v6, v6, v9, v2
	v_lshlrev_b32_e32 v2, 1, v8
	v_lshrrev_b32_e32 v9, 2, v8
	v_and_b32_e32 v10, 3, v10
	s_add_u32 s42, s44, 0x900000
	v_and_b32_e32 v3, 32, v3
	v_bfe_i32 v1, v1, 0, 16
	v_and_b32_e32 v5, 32, v5
	v_and_b32_e32 v2, 24, v2
	v_and_b32_e32 v9, 4, v9
	v_and_or_b32 v10, v8, s3, v10
	s_addc_u32 s43, s45, 0
	v_or3_b32 v9, v10, v9, v2
	v_add_lshl_u32 v2, v3, v1, 1
	s_mov_b32 s3, 0x12000
	v_add_lshl_u32 v4, v5, v4, 1
	s_add_u32 s40, s38, 0x30000
	s_movk_i32 s14, 0x600
	v_mad_u32_u24 v134, v6, s3, v2
	v_mad_u32_u24 v135, v9, s3, v4
	s_addc_u32 s41, s39, 0
	v_mad_u64_u32 v[128:129], s[8:9], v7, s14, v[2:3]
	v_mad_u64_u32 v[130:131], s[8:9], v8, s14, v[4:5]
	s_add_i32 s48, s33, 0
	s_mov_b64 s[8:9], s[44:45]
	v_mov_b32_e32 v1, v135
	v_mov_b32_e32 v2, v134
	s_add_i32 m0, s48, 0x10000
	s_add_i32 s49, s48, 0x2000
	global_load_lds_dwordx4 v2, s[8:9]
	s_add_i32 m0, s48, 0x12000
	v_mov_b32_e32 v2, v135
	global_load_lds_dwordx4 v1, s[8:9]
	v_mov_b32_e32 v1, v134
	s_mov_b64 s[8:9], s[42:43]
	s_add_i32 m0, s48, 0x14000
	s_add_i32 s50, s48, 0x4000
	global_load_lds_dwordx4 v1, s[8:9]
	s_add_i32 m0, s48, 0x16000
	v_mov_b32_e32 v1, v130
	global_load_lds_dwordx4 v2, s[8:9]
	s_mov_b64 s[8:9], s[38:39]
	v_mov_b32_e32 v2, v128
	s_mov_b32 m0, s48
	s_add_i32 s51, s48, 0x6000
	global_load_lds_dwordx4 v2, s[8:9]
	s_mov_b32 m0, s49
	v_mov_b32_e32 v2, v130
	global_load_lds_dwordx4 v1, s[8:9]
	v_mov_b32_e32 v1, v128
	s_mov_b64 s[8:9], s[40:41]
	s_mov_b32 m0, s50
	s_cmp_eq_u32 s7, 1
	global_load_lds_dwordx4 v1, s[8:9]
	s_mov_b32 m0, s51
	s_movk_i32 s52, 0x2000
	global_load_lds_dwordx4 v2, s[8:9]
	s_mov_b32 s54, 0
	s_mov_b32 s53, 0x10000
	s_mov_b32 s55, 0x14000
	s_movk_i32 s56, 0x4000
	s_cselect_b64 s[8:9], -1, 0
	s_cmp_lg_u32 s7, 1
	s_movk_i32 s57, 0x6000
	s_cbranch_scc1 .LBB0_1242
	s_barrier
.LBB0_1242:
	s_lshl_b32 s10, s10, 5
	s_and_b32 s17, s10, 0x60
	s_lshl_b32 s16, s7, 13
	s_lshl_b32 s18, s17, 7
	s_add_u32 s58, s26, 0x75000000
	s_addc_u32 s59, s27, 0
	s_lshl_b32 s10, s11, 1
	s_or_b32 s10, s10, s13
	s_mul_i32 s10, s10, 9
	s_add_i32 s10, s10, s12
	s_ashr_i32 s11, s10, 31
	s_lshl_b64 s[10:11], s[10:11], 17
	s_add_u32 s22, s58, s10
	s_addc_u32 s23, s59, s11
	s_add_u32 s10, s44, 0x80
	s_addc_u32 s11, s45, 0
	s_add_u32 s12, s38, 0x80
	s_addc_u32 s13, s39, 0
	s_add_u32 s14, s44, 0x900080
	s_addc_u32 s15, s45, 0
	v_mov_b32_e32 v1, v134
	v_mov_b32_e32 v2, v135
	s_add_i32 m0, s48, 0x18000
	s_waitcnt vmcnt(2)
	s_barrier
	s_add_i32 s60, s48, 0x8000
	global_load_lds_dwordx4 v1, s[10:11]
	s_add_i32 m0, s48, 0x1a000
	v_mov_b32_e32 v1, v130
	global_load_lds_dwordx4 v2, s[10:11]
	v_mov_b32_e32 v2, v128
	s_mov_b32 m0, s60
	s_add_i32 s61, s48, 0xa000
	v_mov_b64_e32 v[132:133], 0x47f
	global_load_lds_dwordx4 v2, s[12:13]
	s_mov_b32 m0, s61
	v_mov_b32_e32 v2, v134
	global_load_lds_dwordx4 v1, s[12:13]
	v_mov_b32_e32 v1, v135
	s_add_i32 m0, s48, 0x1c000
	s_nop 0
	global_load_lds_dwordx4 v2, s[14:15]
	s_add_i32 m0, s48, 0x1e000
	v_lshrrev_b32_e32 v2, 1, v0
	global_load_lds_dwordx4 v1, s[14:15]
	v_and_b32_e32 v2, 24, v2
	s_cmp_gt_i32 s2, 0
	v_and_b32_e32 v1, 15, v0
	v_lshlrev_b32_e32 v3, 1, v2
	v_lshlrev_b32_e32 v0, 2, v0
	s_cselect_b64 s[10:11], -1, 0
	s_add_i32 s62, s2, -2
	v_lshl_or_b32 v129, s7, 6, v1
	v_lshl_or_b32 v1, v1, 6, v3
	v_and_b32_e32 v0, 32, v0
	s_waitcnt vmcnt(6)
	s_cmpk_lt_u32 s6, 0x100
	v_bitop3_b32 v3, v1, s16, v0 bitop3:0xde
	v_bitop3_b32 v131, v1, s18, v0 bitop3:0xde
	s_cselect_b64 s[12:13], -1, 0
	s_add_i32 s63, 0, 0x10000
	s_add_i32 s64, 0, 0x14000
	v_or_b32_e32 v136, s17, v2
	v_add_u32_e32 v137, s63, v131
	v_add_u32_e32 v138, s64, v131
	v_add_u32_e32 v139, 0, v3
	s_barrier
	s_branch .LBB0_1245

.LBB0_1252:
	ds_read_b128 v[140:143], v137
	ds_read_b128 v[144:147], v137 offset:1024
	ds_read_b128 v[148:151], v137 offset:2048
	ds_read_b128 v[152:155], v137 offset:3072
	ds_read_b128 v[156:159], v138
	ds_read_b128 v[160:163], v138 offset:1024
	ds_read_b128 v[164:167], v138 offset:2048
	ds_read_b128 v[168:171], v138 offset:3072
	s_add_i32 s73, s38, 2
	s_add_u32 s44, s71, 0xffffff80
	s_addc_u32 s45, s72, -1
	s_add_i32 m0, s48, 0xc000
	s_add_i32 s74, s48, 0xe000
	s_cmp_eq_u32 s62, s38
	s_cselect_b32 s38, s36, s69
	s_cselect_b32 s39, s37, s70
	s_cselect_b32 s41, s35, s66
	s_cselect_b32 s40, s34, s65
	s_cselect_b32 s43, s29, s72
	s_cselect_b32 s42, s28, s71
	v_mov_b32_e32 v204, v130
	v_mov_b32_e32 v205, v128
	ds_read_b128 v[172:175], v139
	ds_read_b128 v[176:179], v139 offset:1024
	ds_read_b128 v[180:183], v139 offset:2048
	ds_read_b128 v[184:187], v139 offset:3072
	ds_read_b128 v[188:191], v139 offset:4096
	ds_read_b128 v[192:195], v139 offset:5120
	ds_read_b128 v[196:199], v139 offset:6144
	ds_read_b128 v[200:203], v139 offset:7168
	s_nop 0
	global_load_lds_dwordx4 v205, s[44:45]
	s_mov_b32 m0, s74
	s_nop 0
	global_load_lds_dwordx4 v204, s[44:45]
	s_waitcnt vmcnt(8)
	s_waitcnt lgkmcnt(0)
	s_barrier
	s_setprio 1
	s_waitcnt lgkmcnt(0)
	v_mfma_f32_16x16x32_bf16 v[124:127], v[140:143], v[172:175], v[124:127]
	v_mfma_f32_16x16x32_bf16 v[120:123], v[148:151], v[172:175], v[120:123]
	v_mfma_f32_16x16x32_bf16 v[108:111], v[140:143], v[180:183], v[108:111]
	v_mfma_f32_16x16x32_bf16 v[104:107], v[148:151], v[180:183], v[104:107]
	v_mfma_f32_16x16x32_bf16 v[92:95], v[140:143], v[188:191], v[92:95]
	v_mfma_f32_16x16x32_bf16 v[88:91], v[148:151], v[188:191], v[88:91]
	v_mfma_f32_16x16x32_bf16 v[76:79], v[140:143], v[196:199], v[76:79]
	v_mfma_f32_16x16x32_bf16 v[72:75], v[148:151], v[196:199], v[72:75]
	v_mfma_f32_16x16x32_bf16 v[124:127], v[144:147], v[176:179], v[124:127]
	v_mfma_f32_16x16x32_bf16 v[120:123], v[152:155], v[176:179], v[120:123]
	v_mfma_f32_16x16x32_bf16 v[108:111], v[144:147], v[184:187], v[108:111]
	v_mfma_f32_16x16x32_bf16 v[104:107], v[152:155], v[184:187], v[104:107]
	v_mfma_f32_16x16x32_bf16 v[92:95], v[144:147], v[192:195], v[92:95]
	v_mfma_f32_16x16x32_bf16 v[88:91], v[152:155], v[192:195], v[88:91]
	v_mfma_f32_16x16x32_bf16 v[76:79], v[144:147], v[200:203], v[76:79]
	v_mfma_f32_16x16x32_bf16 v[72:75], v[152:155], v[200:203], v[72:75]
	s_setprio 0
	s_setprio 1
	v_mfma_f32_16x16x32_bf16 v[116:119], v[156:159], v[172:175], v[116:119]
	v_mfma_f32_16x16x32_bf16 v[112:115], v[164:167], v[172:175], v[112:115]
	v_mfma_f32_16x16x32_bf16 v[100:103], v[156:159], v[180:183], v[100:103]
	v_mfma_f32_16x16x32_bf16 v[96:99], v[164:167], v[180:183], v[96:99]
	v_mfma_f32_16x16x32_bf16 v[84:87], v[156:159], v[188:191], v[84:87]
	v_mfma_f32_16x16x32_bf16 v[80:83], v[164:167], v[188:191], v[80:83]
	v_mfma_f32_16x16x32_bf16 v[68:71], v[156:159], v[196:199], v[68:71]
	v_mfma_f32_16x16x32_bf16 v[60:63], v[164:167], v[196:199], v[60:63]
	v_mfma_f32_16x16x32_bf16 v[116:119], v[160:163], v[176:179], v[116:119]
	v_mfma_f32_16x16x32_bf16 v[112:115], v[168:171], v[176:179], v[112:115]
	v_mfma_f32_16x16x32_bf16 v[100:103], v[160:163], v[184:187], v[100:103]
	v_mfma_f32_16x16x32_bf16 v[96:99], v[168:171], v[184:187], v[96:99]
	v_mfma_f32_16x16x32_bf16 v[84:87], v[160:163], v[192:195], v[84:87]
	v_mfma_f32_16x16x32_bf16 v[80:83], v[168:171], v[192:195], v[80:83]
	v_mfma_f32_16x16x32_bf16 v[68:71], v[160:163], v[200:203], v[68:71]
	v_mfma_f32_16x16x32_bf16 v[60:63], v[168:171], v[200:203], v[60:63]
	s_setprio 0
	s_barrier
	s_cselect_b32 s45, s31, s68
	s_cselect_b32 s44, s30, s67
	s_add_i32 s76, s63, s33
	v_mov_b32_e32 v204, v134
	s_mov_b64 s[74:75], s[40:41]
	v_mov_b32_e32 v205, v135
	s_mov_b32 m0, s76
	ds_read_b128 v[172:175], v139 offset:16384
	ds_read_b128 v[176:179], v139 offset:17408
	ds_read_b128 v[180:183], v139 offset:18432
	ds_read_b128 v[184:187], v139 offset:19456
	ds_read_b128 v[188:191], v139 offset:20480
	ds_read_b128 v[192:195], v139 offset:21504
	ds_read_b128 v[196:199], v139 offset:22528
	ds_read_b128 v[200:203], v139 offset:23552
	s_nop 0
	global_load_lds_dwordx4 v204, s[74:75]
	s_add_i32 m0, s76, 0x2000
	s_add_i32 s76, s64, s33
	global_load_lds_dwordx4 v205, s[74:75]
	v_mov_b32_e32 v204, v134
	v_mov_b32_e32 v205, v135
	s_mov_b64 s[74:75], s[44:45]
	s_mov_b32 m0, s76
	s_nop 0
	global_load_lds_dwordx4 v204, s[74:75]
	s_add_i32 m0, s76, 0x2000
	v_mov_b32_e32 v204, v130
	global_load_lds_dwordx4 v205, s[74:75]
	s_mov_b64 s[74:75], s[38:39]
	v_mov_b32_e32 v205, v128
	s_mov_b32 m0, s48
	s_nop 0
	global_load_lds_dwordx4 v205, s[74:75]
	s_mov_b32 m0, s49
	s_nop 0
	global_load_lds_dwordx4 v204, s[74:75]
	s_waitcnt vmcnt(8)
	s_waitcnt lgkmcnt(0)
	s_barrier
	s_setprio 1
	s_waitcnt lgkmcnt(0)
	v_mfma_f32_16x16x32_bf16 v[64:67], v[140:143], v[172:175], v[64:67]
	v_mfma_f32_16x16x32_bf16 v[56:59], v[148:151], v[172:175], v[56:59]
	v_mfma_f32_16x16x32_bf16 v[44:47], v[140:143], v[180:183], v[44:47]
	v_mfma_f32_16x16x32_bf16 v[40:43], v[148:151], v[180:183], v[40:43]
	v_mfma_f32_16x16x32_bf16 v[28:31], v[140:143], v[188:191], v[28:31]
	v_mfma_f32_16x16x32_bf16 v[24:27], v[148:151], v[188:191], v[24:27]
	v_mfma_f32_16x16x32_bf16 v[12:15], v[140:143], v[196:199], v[12:15]
	v_mfma_f32_16x16x32_bf16 v[8:11], v[148:151], v[196:199], v[8:11]
	v_mfma_f32_16x16x32_bf16 v[64:67], v[144:147], v[176:179], v[64:67]
	v_mfma_f32_16x16x32_bf16 v[56:59], v[152:155], v[176:179], v[56:59]
	v_mfma_f32_16x16x32_bf16 v[44:47], v[144:147], v[184:187], v[44:47]
	v_mfma_f32_16x16x32_bf16 v[40:43], v[152:155], v[184:187], v[40:43]
	v_mfma_f32_16x16x32_bf16 v[28:31], v[144:147], v[192:195], v[28:31]
	v_mfma_f32_16x16x32_bf16 v[24:27], v[152:155], v[192:195], v[24:27]
	v_mfma_f32_16x16x32_bf16 v[12:15], v[144:147], v[200:203], v[12:15]
	v_mfma_f32_16x16x32_bf16 v[8:11], v[152:155], v[200:203], v[8:11]
	s_setprio 0
	s_setprio 1
	v_mfma_f32_16x16x32_bf16 v[52:55], v[156:159], v[172:175], v[52:55]
	v_mfma_f32_16x16x32_bf16 v[48:51], v[164:167], v[172:175], v[48:51]
	v_mfma_f32_16x16x32_bf16 v[36:39], v[156:159], v[180:183], v[36:39]
	v_mfma_f32_16x16x32_bf16 v[32:35], v[164:167], v[180:183], v[32:35]
	v_mfma_f32_16x16x32_bf16 v[20:23], v[156:159], v[188:191], v[20:23]
	v_mfma_f32_16x16x32_bf16 v[16:19], v[164:167], v[188:191], v[16:19]
	v_mfma_f32_16x16x32_bf16 v[4:7], v[156:159], v[196:199], v[4:7]
	v_mfma_f32_16x16x32_bf16 v[0:3], v[164:167], v[196:199], v[0:3]
	v_mfma_f32_16x16x32_bf16 v[52:55], v[160:163], v[176:179], v[52:55]
	v_mfma_f32_16x16x32_bf16 v[48:51], v[168:171], v[176:179], v[48:51]
	v_mfma_f32_16x16x32_bf16 v[36:39], v[160:163], v[184:187], v[36:39]
	v_mfma_f32_16x16x32_bf16 v[32:35], v[168:171], v[184:187], v[32:35]
	v_mfma_f32_16x16x32_bf16 v[20:23], v[160:163], v[192:195], v[20:23]
	v_mfma_f32_16x16x32_bf16 v[16:19], v[168:171], v[192:195], v[16:19]
	v_mfma_f32_16x16x32_bf16 v[4:7], v[160:163], v[200:203], v[4:7]
	v_mfma_f32_16x16x32_bf16 v[0:3], v[168:171], v[200:203], v[0:3]
	s_setprio 0
	s_barrier
	s_add_i32 s74, 0, 0x18000
	s_add_i32 s75, 0, 0x1c000
	v_add_u32_e32 v152, s74, v131
	v_add_u32_e32 v168, s75, v131
	ds_read_b128 v[140:143], v152
	ds_read_b128 v[144:147], v152 offset:1024
	ds_read_b128 v[148:151], v152 offset:2048
	ds_read_b128 v[152:155], v152 offset:3072
	ds_read_b128 v[156:159], v168
	ds_read_b128 v[160:163], v168 offset:1024
	ds_read_b128 v[164:167], v168 offset:2048
	ds_read_b128 v[168:171], v168 offset:3072
	v_mov_b32_e32 v204, v130
	v_mov_b32_e32 v205, v128
	s_mov_b32 m0, s50
	ds_read_b128 v[172:175], v139 offset:32768
	ds_read_b128 v[176:179], v139 offset:33792
	ds_read_b128 v[180:183], v139 offset:34816
	ds_read_b128 v[184:187], v139 offset:35840
	ds_read_b128 v[188:191], v139 offset:36864
	ds_read_b128 v[192:195], v139 offset:37888
	ds_read_b128 v[196:199], v139 offset:38912
	ds_read_b128 v[200:203], v139 offset:39936
	s_nop 0
	global_load_lds_dwordx4 v205, s[42:43]
	s_mov_b32 m0, s51
	s_nop 0
	global_load_lds_dwordx4 v204, s[42:43]
	s_waitcnt vmcnt(8)
	s_waitcnt lgkmcnt(0)
	s_barrier
	s_setprio 1
	s_waitcnt lgkmcnt(0)
	v_mfma_f32_16x16x32_bf16 v[124:127], v[140:143], v[172:175], v[124:127]
	v_mfma_f32_16x16x32_bf16 v[120:123], v[148:151], v[172:175], v[120:123]
	v_mfma_f32_16x16x32_bf16 v[108:111], v[140:143], v[180:183], v[108:111]
	v_mfma_f32_16x16x32_bf16 v[104:107], v[148:151], v[180:183], v[104:107]
	v_mfma_f32_16x16x32_bf16 v[92:95], v[140:143], v[188:191], v[92:95]
	v_mfma_f32_16x16x32_bf16 v[88:91], v[148:151], v[188:191], v[88:91]
	v_mfma_f32_16x16x32_bf16 v[76:79], v[140:143], v[196:199], v[76:79]
	v_mfma_f32_16x16x32_bf16 v[72:75], v[148:151], v[196:199], v[72:75]
	v_mfma_f32_16x16x32_bf16 v[124:127], v[144:147], v[176:179], v[124:127]
	v_mfma_f32_16x16x32_bf16 v[120:123], v[152:155], v[176:179], v[120:123]
	v_mfma_f32_16x16x32_bf16 v[108:111], v[144:147], v[184:187], v[108:111]
	v_mfma_f32_16x16x32_bf16 v[104:107], v[152:155], v[184:187], v[104:107]
	v_mfma_f32_16x16x32_bf16 v[92:95], v[144:147], v[192:195], v[92:95]
	v_mfma_f32_16x16x32_bf16 v[88:91], v[152:155], v[192:195], v[88:91]
	v_mfma_f32_16x16x32_bf16 v[76:79], v[144:147], v[200:203], v[76:79]
	v_mfma_f32_16x16x32_bf16 v[72:75], v[152:155], v[200:203], v[72:75]
	s_setprio 0
	s_setprio 1
	v_mfma_f32_16x16x32_bf16 v[116:119], v[156:159], v[172:175], v[116:119]
	v_mfma_f32_16x16x32_bf16 v[112:115], v[164:167], v[172:175], v[112:115]
	v_mfma_f32_16x16x32_bf16 v[100:103], v[156:159], v[180:183], v[100:103]
	v_mfma_f32_16x16x32_bf16 v[96:99], v[164:167], v[180:183], v[96:99]
	v_mfma_f32_16x16x32_bf16 v[84:87], v[156:159], v[188:191], v[84:87]
	v_mfma_f32_16x16x32_bf16 v[80:83], v[164:167], v[188:191], v[80:83]
	v_mfma_f32_16x16x32_bf16 v[68:71], v[156:159], v[196:199], v[68:71]
	v_mfma_f32_16x16x32_bf16 v[60:63], v[164:167], v[196:199], v[60:63]
	v_mfma_f32_16x16x32_bf16 v[116:119], v[160:163], v[176:179], v[116:119]
	v_mfma_f32_16x16x32_bf16 v[112:115], v[168:171], v[176:179], v[112:115]
	v_mfma_f32_16x16x32_bf16 v[100:103], v[160:163], v[184:187], v[100:103]
	v_mfma_f32_16x16x32_bf16 v[96:99], v[168:171], v[184:187], v[96:99]
	v_mfma_f32_16x16x32_bf16 v[84:87], v[160:163], v[192:195], v[84:87]
	v_mfma_f32_16x16x32_bf16 v[80:83], v[168:171], v[192:195], v[80:83]
	v_mfma_f32_16x16x32_bf16 v[68:71], v[160:163], v[200:203], v[68:71]
	v_mfma_f32_16x16x32_bf16 v[60:63], v[168:171], v[200:203], v[60:63]
	s_setprio 0
	s_barrier
	s_add_u32 s40, s40, 0x80
	s_addc_u32 s41, s41, 0
	s_add_i32 s42, s74, s33
	v_mov_b32_e32 v204, v134
	v_mov_b32_e32 v205, v135
	s_mov_b32 m0, s42
	ds_read_b128 v[172:175], v139 offset:49152
	ds_read_b128 v[176:179], v139 offset:50176
	ds_read_b128 v[180:183], v139 offset:51200
	ds_read_b128 v[184:187], v139 offset:52224
	ds_read_b128 v[188:191], v139 offset:53248
	ds_read_b128 v[192:195], v139 offset:54272
	ds_read_b128 v[196:199], v139 offset:55296
	ds_read_b128 v[200:203], v139 offset:56320
	s_nop 0
	global_load_lds_dwordx4 v204, s[40:41]
	s_add_i32 m0, s42, 0x2000
	v_mov_b32_e32 v204, v134
	global_load_lds_dwordx4 v205, s[40:41]
	s_add_u32 s40, s44, 0x80
	s_addc_u32 s41, s45, 0
	s_add_i32 s42, s75, s33
	v_mov_b32_e32 v205, v135
	s_mov_b32 m0, s42
	s_nop 0
	global_load_lds_dwordx4 v204, s[40:41]
	s_add_i32 m0, s42, 0x2000
	s_add_u32 s38, s38, 0x80
	global_load_lds_dwordx4 v205, s[40:41]
	s_addc_u32 s39, s39, 0
	v_mov_b32_e32 v204, v130
	v_mov_b32_e32 v205, v128
	s_mov_b32 m0, s60
	s_nop 0
	global_load_lds_dwordx4 v205, s[38:39]
	s_mov_b32 m0, s61
	s_nop 0
	global_load_lds_dwordx4 v204, s[38:39]
	s_waitcnt vmcnt(8)
	s_waitcnt lgkmcnt(0)
	s_barrier
	s_setprio 1
	s_waitcnt lgkmcnt(0)
	v_mfma_f32_16x16x32_bf16 v[64:67], v[140:143], v[172:175], v[64:67]
	v_mfma_f32_16x16x32_bf16 v[56:59], v[148:151], v[172:175], v[56:59]
	v_mfma_f32_16x16x32_bf16 v[44:47], v[140:143], v[180:183], v[44:47]
	v_mfma_f32_16x16x32_bf16 v[40:43], v[148:151], v[180:183], v[40:43]
	v_mfma_f32_16x16x32_bf16 v[28:31], v[140:143], v[188:191], v[28:31]
	v_mfma_f32_16x16x32_bf16 v[24:27], v[148:151], v[188:191], v[24:27]
	v_mfma_f32_16x16x32_bf16 v[12:15], v[140:143], v[196:199], v[12:15]
	v_mfma_f32_16x16x32_bf16 v[8:11], v[148:151], v[196:199], v[8:11]
	v_mfma_f32_16x16x32_bf16 v[64:67], v[144:147], v[176:179], v[64:67]
	v_mfma_f32_16x16x32_bf16 v[56:59], v[152:155], v[176:179], v[56:59]
	v_mfma_f32_16x16x32_bf16 v[44:47], v[144:147], v[184:187], v[44:47]
	v_mfma_f32_16x16x32_bf16 v[40:43], v[152:155], v[184:187], v[40:43]
	v_mfma_f32_16x16x32_bf16 v[28:31], v[144:147], v[192:195], v[28:31]
	v_mfma_f32_16x16x32_bf16 v[24:27], v[152:155], v[192:195], v[24:27]
	v_mfma_f32_16x16x32_bf16 v[12:15], v[144:147], v[200:203], v[12:15]
	v_mfma_f32_16x16x32_bf16 v[8:11], v[152:155], v[200:203], v[8:11]
	s_setprio 0
	s_setprio 1
	v_mfma_f32_16x16x32_bf16 v[52:55], v[156:159], v[172:175], v[52:55]
	v_mfma_f32_16x16x32_bf16 v[48:51], v[164:167], v[172:175], v[48:51]
	v_mfma_f32_16x16x32_bf16 v[36:39], v[156:159], v[180:183], v[36:39]
	v_mfma_f32_16x16x32_bf16 v[32:35], v[164:167], v[180:183], v[32:35]
	v_mfma_f32_16x16x32_bf16 v[20:23], v[156:159], v[188:191], v[20:23]
	v_mfma_f32_16x16x32_bf16 v[16:19], v[164:167], v[188:191], v[16:19]
	v_mfma_f32_16x16x32_bf16 v[4:7], v[156:159], v[196:199], v[4:7]
	v_mfma_f32_16x16x32_bf16 v[0:3], v[164:167], v[196:199], v[0:3]
	v_mfma_f32_16x16x32_bf16 v[52:55], v[160:163], v[176:179], v[52:55]
	v_mfma_f32_16x16x32_bf16 v[48:51], v[168:171], v[176:179], v[48:51]
	v_mfma_f32_16x16x32_bf16 v[36:39], v[160:163], v[184:187], v[36:39]
	v_mfma_f32_16x16x32_bf16 v[32:35], v[168:171], v[184:187], v[32:35]
	v_mfma_f32_16x16x32_bf16 v[20:23], v[160:163], v[192:195], v[20:23]
	v_mfma_f32_16x16x32_bf16 v[16:19], v[168:171], v[192:195], v[16:19]
	v_mfma_f32_16x16x32_bf16 v[4:7], v[160:163], v[200:203], v[4:7]
	v_mfma_f32_16x16x32_bf16 v[0:3], v[168:171], v[200:203], v[0:3]
	s_setprio 0
	s_barrier
	s_add_u32 s65, s65, 0x100
	s_addc_u32 s66, s66, 0
	s_add_u32 s67, s67, 0x100
	s_addc_u32 s68, s68, 0
	s_add_u32 s69, s69, 0x100
	s_addc_u32 s70, s70, 0
	s_add_u32 s71, s71, 0x100
	s_addc_u32 s72, s72, 0
	s_cmp_ge_i32 s73, s2
	s_mov_b32 s38, s73
	s_cbranch_scc0 .LBB0_1252
	s_and_b64 vcc, exec, s[12:13]
	s_cbranch_vccz .LBB0_1255

.LBB0_1421:
	v_ashrrev_i32_e32 v3, 31, v1
	v_lshrrev_b32_e32 v3, 26, v3
	v_lshlrev_b32_e32 v2, 4, v1
	v_add_u32_e32 v3, v1, v3
	v_bfe_i32 v1, v1, 27, 1
	v_lshrrev_b32_e32 v1, 22, v1
	v_add_u32_e32 v1, v2, v1
	v_and_b32_e32 v1, 0xfffffc00, v1
	v_sub_u32_e32 v1, v2, v1
	v_lshrrev_b32_e32 v4, 4, v1
	v_bitop3_b32 v1, v4, v1, 32 bitop3:0x6c
	v_ashrrev_i32_e32 v5, 31, v1
	v_ashrrev_i32_e32 v3, 6, v3
	v_lshrrev_b32_e32 v5, 26, v5
	v_lshlrev_b32_e32 v4, 3, v3
	v_add_u32_e32 v5, v1, v5
	v_and_b32_e32 v4, -16, v4
	v_ashrrev_i32_e32 v6, 6, v5
	v_add_u32_e32 v2, 0x2000, v2
	v_add_u32_e32 v7, v6, v4
	v_and_b32_e32 v4, 0xc0, v5
	v_ashrrev_i32_e32 v5, 31, v2
	v_lshrrev_b32_e32 v5, 22, v5
	v_add_u32_e32 v5, v2, v5
	v_ashrrev_i32_e32 v5, 10, v5
	v_mul_i32_i24_e32 v8, 0x400, v5
	v_sub_u32_e32 v2, v2, v8
	v_lshrrev_b32_e32 v8, 4, v2
	v_bitop3_b32 v2, v8, v2, 32 bitop3:0x6c
	v_ashrrev_i32_e32 v9, 31, v2
	v_lshrrev_b32_e32 v9, 26, v9
	v_add_u32_e32 v9, v2, v9
	v_ashrrev_i32_e32 v10, 6, v9
	v_and_b32_e32 v9, 0xc0, v9
	v_sub_u32_e32 v1, v1, v4
	v_mov_b32_e32 v4, 1
	v_sub_u32_e32 v2, v2, v9
	v_lshlrev_b32_e32 v8, 3, v5
	v_ashrrev_i16_sdwa v2, v4, sext(v2) dst_sel:DWORD dst_unused:UNUSED_PAD src0_sel:DWORD src1_sel:BYTE_0
	v_ashrrev_i16_sdwa v1, v4, sext(v1) dst_sel:DWORD dst_unused:UNUSED_PAD src0_sel:DWORD src1_sel:BYTE_0
	v_and_b32_e32 v8, -16, v8
	v_bfe_i32 v4, v2, 0, 16
	v_lshlrev_b32_e32 v2, 1, v7
	v_lshrrev_b32_e32 v9, 2, v7
	v_and_b32_e32 v6, 3, v6
	s_mov_b32 s9, 0x7fffe0
	v_add_u32_e32 v8, v10, v8
	v_and_b32_e32 v2, 24, v2
	v_and_b32_e32 v9, 4, v9
	v_and_or_b32 v6, v7, s9, v6
	s_ashr_i32 s7, s8, 6
	v_lshlrev_b32_e32 v3, 5, v3
	v_lshlrev_b32_e32 v5, 5, v5
	v_or3_b32 v6, v6, v9, v2
	v_lshlrev_b32_e32 v2, 1, v8
	v_lshrrev_b32_e32 v9, 2, v8
	v_and_b32_e32 v10, 3, v10
	s_ashr_i32 s6, s8, 8
	v_and_b32_e32 v3, 32, v3
	v_bfe_i32 v1, v1, 0, 16
	v_and_b32_e32 v5, 32, v5
	v_and_b32_e32 v2, 24, v2
	v_and_b32_e32 v9, 4, v9
	v_and_or_b32 v10, v8, s9, v10
	s_lshl_b32 s31, s7, 10
	v_or3_b32 v9, v10, v9, v2
	v_add_lshl_u32 v2, v3, v1, 1
	s_movk_i32 s9, 0x600
	v_add_lshl_u32 v4, v5, v4, 1
	s_add_u32 s52, s12, 0x30000
	v_mad_u32_u24 v214, v6, s9, v2
	v_mad_u32_u24 v215, v9, s9, v4
	v_mad_u64_u32 v[204:205], s[10:11], v7, s9, v[2:3]
	v_mad_u64_u32 v[206:207], s[10:11], v8, s9, v[4:5]
	s_addc_u32 s53, s13, 0
	s_add_i32 s33, s31, 0
	v_mov_b32_e32 v1, v214
	s_mov_b64 s[10:11], s[50:51]
	v_mov_b32_e32 v2, v215
	s_add_i32 m0, s33, 0x10000
	s_add_i32 s54, s33, 0x2000
	global_load_lds_dwordx4 v1, s[10:11]
	s_add_i32 m0, s33, 0x12000
	v_mov_b32_e32 v1, v214
	global_load_lds_dwordx4 v2, s[10:11]
	s_mov_b64 s[10:11], s[48:49]
	v_mov_b32_e32 v2, v215
	s_add_i32 m0, s33, 0x14000
	s_add_i32 s55, s33, 0x4000
	global_load_lds_dwordx4 v1, s[10:11]
	s_add_i32 m0, s33, 0x16000
	v_mov_b32_e32 v1, v206
	global_load_lds_dwordx4 v2, s[10:11]
	s_mov_b64 s[10:11], s[12:13]
	v_mov_b32_e32 v2, v204
	s_mov_b32 m0, s33
	s_add_i32 s56, s33, 0x6000
	global_load_lds_dwordx4 v2, s[10:11]
	s_mov_b32 m0, s54
	v_mov_b32_e32 v2, v206
	global_load_lds_dwordx4 v1, s[10:11]
	v_mov_b32_e32 v1, v204
	s_mov_b64 s[10:11], s[52:53]
	s_mov_b32 m0, s55
	s_cmp_eq_u32 s6, 1
	global_load_lds_dwordx4 v1, s[10:11]
	s_mov_b32 m0, s56
	s_cselect_b64 s[16:17], -1, 0
	global_load_lds_dwordx4 v2, s[10:11]
	s_cmp_lg_u32 s6, 1
	s_mov_b32 s18, 0
	s_cbranch_scc1 .LBB0_1423
	s_barrier
.LBB0_1423:
	s_and_b32 s19, s7, 3
	s_load_dword s10, s[90:91], 0x100
	s_lshl_b32 s7, s6, 13
	s_lshl_b32 s9, s19, 12
	s_add_u32 s57, s26, 0x4e000000
	s_addc_u32 s58, s27, 0
	s_add_u32 s20, s26, 0x63800000
	s_addc_u32 s21, s27, 0
	s_waitcnt lgkmcnt(0)
	s_ashr_i32 s59, s10, 31
	s_add_u32 s10, s50, 0x80
	s_addc_u32 s11, s51, 0
	v_mov_b32_e32 v1, v214
	v_mov_b32_e32 v2, v215
	s_add_i32 m0, s33, 0x18000
	s_waitcnt vmcnt(2)
	s_barrier
	v_mov_b32_e32 v208, 0
	global_load_lds_dwordx4 v1, s[10:11]
	s_add_i32 m0, s33, 0x1a000
	v_mov_b32_e32 v1, v206
	global_load_lds_dwordx4 v2, s[10:11]
	s_add_u32 s10, s12, 0x80
	s_addc_u32 s11, s13, 0
	s_add_i32 s60, s33, 0x8000
	v_mov_b32_e32 v2, v204
	s_mov_b32 m0, s60
	s_add_i32 s61, s33, 0xa000
	s_mov_b32 s30, 0x3b800000
	global_load_lds_dwordx4 v2, s[10:11]
	s_mov_b32 m0, s61
	v_mov_b32_e32 v2, v215
	global_load_lds_dwordx4 v1, s[10:11]
	s_add_u32 s10, s48, 0x80
	s_addc_u32 s11, s49, 0
	v_mov_b32_e32 v1, v214
	s_add_i32 m0, s33, 0x1c000
	s_mov_b32 s73, 0xf800000
	global_load_lds_dwordx4 v1, s[10:11]
	s_add_i32 m0, s33, 0x1e000
	s_cmp_gt_i32 s3, 0
	global_load_lds_dwordx4 v2, s[10:11]
	v_bfe_u32 v2, v0, 4, 2
	s_cselect_b64 s[22:23], -1, 0
	s_add_i32 s62, s3, -2
	v_and_b32_e32 v1, 15, v0
	v_lshlrev_b32_e32 v4, 4, v2
	v_lshlrev_b32_e32 v0, 2, v0
	s_cmpk_lt_u32 s8, 0x100
	v_lshl_or_b32 v205, s6, 6, v1
	v_lshl_or_b32 v1, v1, 6, v4
	v_and_b32_e32 v0, 32, v0
	s_waitcnt vmcnt(6)
	s_cselect_b64 s[28:29], -1, 0
	s_lshl_b32 s10, s19, 3
	v_lshlrev_b32_e32 v3, 3, v2
	v_bitop3_b32 v4, v1, s7, v0 bitop3:0xde
	v_bitop3_b32 v207, v1, s9, v0 bitop3:0xde
	s_add_i32 s70, s10, 0
	s_add_i32 s71, 0, 0x10000
	s_add_i32 s72, 0, 0x14000
	v_mbcnt_lo_u32_b32 v0, -1, 0
	v_lshl_or_b32 v216, s19, 5, v3
	v_cmp_eq_u32_e64 s[6:7], 0, v2
	v_cmp_ne_u32_e64 s[8:9], 0, v2
	s_add_i32 s63, s70, 0x22000
	s_add_i32 s64, s70, 0x22200
	s_add_i32 s65, s70, 0x22400
	s_add_i32 s66, s70, 0x22600
	s_add_i32 s67, s70, 0x23000
	s_add_i32 s68, s70, 0x23200
	s_add_i32 s69, s70, 0x23400
	s_add_i32 s70, s70, 0x23600
	v_add_u32_e32 v217, s71, v207
	v_add_u32_e32 v218, s72, v207
	v_add_u32_e32 v219, 0, v4
	v_mbcnt_hi_u32_b32 v220, -1, v0
	v_mov_b32_e32 v221, 0x260
	v_mov_b64_e32 v[210:211], 0x1ff
	s_mov_b32 s75, 0
	s_barrier
	s_branch .LBB0_1426

.LBB0_1434:
	ds_read_b128 v[68:71], v217
	ds_read_b128 v[80:83], v217 offset:1024
	ds_read_b128 v[92:95], v217 offset:2048
	ds_read_b128 v[104:107], v217 offset:3072
	ds_read_b128 v[116:119], v218
	ds_read_b128 v[128:131], v218 offset:1024
	ds_read_b128 v[136:139], v218 offset:2048
	ds_read_b128 v[140:143], v218 offset:3072
	s_add_i32 s86, s12, 2
	s_add_u32 s52, s84, 0xffffff80
	s_addc_u32 s53, s85, -1
	s_add_i32 m0, s33, 0xc000
	s_add_i32 s87, s33, 0xe000
	s_cmp_eq_u32 s62, s12
	s_cselect_b32 s12, s46, s82
	s_cselect_b32 s13, s47, s83
	s_cselect_b32 s49, s45, s79
	s_cselect_b32 s48, s44, s78
	s_cselect_b32 s51, s41, s85
	s_cselect_b32 s50, s40, s84
	v_mov_b32_e32 v192, v206
	v_mov_b32_e32 v193, v204
	ds_read_b128 v[144:147], v219
	ds_read_b128 v[148:151], v219 offset:1024
	ds_read_b128 v[156:159], v219 offset:2048
	ds_read_b128 v[168:171], v219 offset:3072
	ds_read_b128 v[176:179], v219 offset:4096
	ds_read_b128 v[180:183], v219 offset:5120
	ds_read_b128 v[184:187], v219 offset:6144
	ds_read_b128 v[188:191], v219 offset:7168
	s_nop 0
	global_load_lds_dwordx4 v193, s[52:53]
	s_mov_b32 m0, s87
	s_nop 0
	global_load_lds_dwordx4 v192, s[52:53]
	s_waitcnt vmcnt(8)
	s_waitcnt lgkmcnt(0)
	s_barrier
	s_setprio 1
	s_waitcnt lgkmcnt(0)
	v_mfma_f32_16x16x32_bf16 v[172:175], v[68:71], v[144:147], v[172:175]
	v_mfma_f32_16x16x32_bf16 v[164:167], v[92:95], v[144:147], v[164:167]
	v_mfma_f32_16x16x32_bf16 v[132:135], v[68:71], v[156:159], v[132:135]
	v_mfma_f32_16x16x32_bf16 v[124:127], v[92:95], v[156:159], v[124:127]
	v_mfma_f32_16x16x32_bf16 v[108:111], v[68:71], v[176:179], v[108:111]
	v_mfma_f32_16x16x32_bf16 v[100:103], v[92:95], v[176:179], v[100:103]
	v_mfma_f32_16x16x32_bf16 v[84:87], v[68:71], v[184:187], v[84:87]
	v_mfma_f32_16x16x32_bf16 v[76:79], v[92:95], v[184:187], v[76:79]
	v_mfma_f32_16x16x32_bf16 v[172:175], v[80:83], v[148:151], v[172:175]
	v_mfma_f32_16x16x32_bf16 v[164:167], v[104:107], v[148:151], v[164:167]
	v_mfma_f32_16x16x32_bf16 v[132:135], v[80:83], v[168:171], v[132:135]
	v_mfma_f32_16x16x32_bf16 v[124:127], v[104:107], v[168:171], v[124:127]
	v_mfma_f32_16x16x32_bf16 v[108:111], v[80:83], v[180:183], v[108:111]
	v_mfma_f32_16x16x32_bf16 v[100:103], v[104:107], v[180:183], v[100:103]
	v_mfma_f32_16x16x32_bf16 v[84:87], v[80:83], v[188:191], v[84:87]
	v_mfma_f32_16x16x32_bf16 v[76:79], v[104:107], v[188:191], v[76:79]
	s_setprio 0
	s_setprio 1
	v_mfma_f32_16x16x32_bf16 v[160:163], v[116:119], v[144:147], v[160:163]
	v_mfma_f32_16x16x32_bf16 v[120:123], v[116:119], v[156:159], v[120:123]
	v_mfma_f32_16x16x32_bf16 v[112:115], v[136:139], v[156:159], v[112:115]
	v_mfma_f32_16x16x32_bf16 v[96:99], v[116:119], v[176:179], v[96:99]
	v_mfma_f32_16x16x32_bf16 v[88:91], v[136:139], v[176:179], v[88:91]
	v_mfma_f32_16x16x32_bf16 v[72:75], v[116:119], v[184:187], v[72:75]
	v_mfma_f32_16x16x32_bf16 v[64:67], v[136:139], v[184:187], v[64:67]
	v_mfma_f32_16x16x32_bf16 v[160:163], v[128:131], v[148:151], v[160:163]
	v_mfma_f32_16x16x32_bf16 v[144:147], v[136:139], v[144:147], v[152:155]
	v_mfma_f32_16x16x32_bf16 v[120:123], v[128:131], v[168:171], v[120:123]
	v_mfma_f32_16x16x32_bf16 v[112:115], v[140:143], v[168:171], v[112:115]
	v_mfma_f32_16x16x32_bf16 v[96:99], v[128:131], v[180:183], v[96:99]
	v_mfma_f32_16x16x32_bf16 v[88:91], v[140:143], v[180:183], v[88:91]
	v_mfma_f32_16x16x32_bf16 v[72:75], v[128:131], v[188:191], v[72:75]
	v_mfma_f32_16x16x32_bf16 v[64:67], v[140:143], v[188:191], v[64:67]
	v_mfma_f32_16x16x32_bf16 v[144:147], v[140:143], v[148:151], v[144:147]
	s_setprio 0
	s_barrier
	s_cselect_b32 s53, s43, s81
	s_cselect_b32 s52, s42, s80
	s_add_i32 s87, s71, s31
	v_mov_b32_e32 v192, v214
	s_mov_b64 s[88:89], s[48:49]
	v_mov_b32_e32 v193, v215
	s_mov_b32 m0, s87
	ds_read_b128 v[148:151], v219 offset:16384
	ds_read_b128 v[152:155], v219 offset:17408
	ds_read_b128 v[156:159], v219 offset:18432
	ds_read_b128 v[168:171], v219 offset:19456
	ds_read_b128 v[176:179], v219 offset:20480
	ds_read_b128 v[180:183], v219 offset:21504
	ds_read_b128 v[184:187], v219 offset:22528
	ds_read_b128 v[188:191], v219 offset:23552
	s_nop 0
	global_load_lds_dwordx4 v192, s[88:89]
	s_add_i32 m0, s87, 0x2000
	s_add_i32 s87, s72, s31
	global_load_lds_dwordx4 v193, s[88:89]
	s_mov_b64 s[88:89], s[52:53]
	v_mov_b32_e32 v192, v214
	v_mov_b32_e32 v193, v215
	s_mov_b32 m0, s87
	s_nop 0
	global_load_lds_dwordx4 v192, s[88:89]
	s_add_i32 m0, s87, 0x2000
	v_mov_b32_e32 v192, v206
	global_load_lds_dwordx4 v193, s[88:89]
	s_mov_b64 s[88:89], s[12:13]
	v_mov_b32_e32 v193, v204
	s_mov_b32 m0, s33
	s_nop 0
	global_load_lds_dwordx4 v193, s[88:89]
	s_mov_b32 m0, s54
	s_nop 0
	global_load_lds_dwordx4 v192, s[88:89]
	s_waitcnt vmcnt(8)
	s_waitcnt lgkmcnt(0)
	s_barrier
	s_setprio 1
	s_waitcnt lgkmcnt(0)
	v_mfma_f32_16x16x32_bf16 v[60:63], v[68:71], v[148:151], v[60:63]
	v_mfma_f32_16x16x32_bf16 v[56:59], v[92:95], v[148:151], v[56:59]
	v_mfma_f32_16x16x32_bf16 v[44:47], v[68:71], v[156:159], v[44:47]
	v_mfma_f32_16x16x32_bf16 v[40:43], v[92:95], v[156:159], v[40:43]
	v_mfma_f32_16x16x32_bf16 v[28:31], v[68:71], v[176:179], v[28:31]
	v_mfma_f32_16x16x32_bf16 v[24:27], v[92:95], v[176:179], v[24:27]
	v_mfma_f32_16x16x32_bf16 v[12:15], v[68:71], v[184:187], v[12:15]
	v_mfma_f32_16x16x32_bf16 v[8:11], v[92:95], v[184:187], v[8:11]
	v_mfma_f32_16x16x32_bf16 v[60:63], v[80:83], v[152:155], v[60:63]
	v_mfma_f32_16x16x32_bf16 v[56:59], v[104:107], v[152:155], v[56:59]
	v_mfma_f32_16x16x32_bf16 v[44:47], v[80:83], v[168:171], v[44:47]
	v_mfma_f32_16x16x32_bf16 v[40:43], v[104:107], v[168:171], v[40:43]
	v_mfma_f32_16x16x32_bf16 v[28:31], v[80:83], v[180:183], v[28:31]
	v_mfma_f32_16x16x32_bf16 v[24:27], v[104:107], v[180:183], v[24:27]
	v_mfma_f32_16x16x32_bf16 v[12:15], v[80:83], v[188:191], v[12:15]
	v_mfma_f32_16x16x32_bf16 v[8:11], v[104:107], v[188:191], v[8:11]
	s_setprio 0
	s_setprio 1
	v_mfma_f32_16x16x32_bf16 v[52:55], v[116:119], v[148:151], v[52:55]
	v_mfma_f32_16x16x32_bf16 v[48:51], v[136:139], v[148:151], v[48:51]
	v_mfma_f32_16x16x32_bf16 v[36:39], v[116:119], v[156:159], v[36:39]
	v_mfma_f32_16x16x32_bf16 v[32:35], v[136:139], v[156:159], v[32:35]
	v_mfma_f32_16x16x32_bf16 v[20:23], v[116:119], v[176:179], v[20:23]
	v_mfma_f32_16x16x32_bf16 v[16:19], v[136:139], v[176:179], v[16:19]
	v_mfma_f32_16x16x32_bf16 v[4:7], v[116:119], v[184:187], v[4:7]
	v_mfma_f32_16x16x32_bf16 v[0:3], v[136:139], v[184:187], v[0:3]
	v_mfma_f32_16x16x32_bf16 v[52:55], v[128:131], v[152:155], v[52:55]
	v_mfma_f32_16x16x32_bf16 v[48:51], v[140:143], v[152:155], v[48:51]
	v_mfma_f32_16x16x32_bf16 v[36:39], v[128:131], v[168:171], v[36:39]
	v_mfma_f32_16x16x32_bf16 v[32:35], v[140:143], v[168:171], v[32:35]
	v_mfma_f32_16x16x32_bf16 v[20:23], v[128:131], v[180:183], v[20:23]
	v_mfma_f32_16x16x32_bf16 v[16:19], v[140:143], v[180:183], v[16:19]
	v_mfma_f32_16x16x32_bf16 v[4:7], v[128:131], v[188:191], v[4:7]
	v_mfma_f32_16x16x32_bf16 v[0:3], v[140:143], v[188:191], v[0:3]
	s_setprio 0
	s_barrier
	s_add_i32 s87, 0, 0x18000
	s_add_i32 s88, 0, 0x1c000
	v_add_u32_e32 v104, s87, v207
	v_add_u32_e32 v140, s88, v207
	ds_read_b128 v[68:71], v104
	ds_read_b128 v[80:83], v104 offset:1024
	ds_read_b128 v[92:95], v104 offset:2048
	ds_read_b128 v[104:107], v104 offset:3072
	ds_read_b128 v[116:119], v140
	ds_read_b128 v[128:131], v140 offset:1024
	ds_read_b128 v[136:139], v140 offset:2048
	ds_read_b128 v[140:143], v140 offset:3072
	v_mov_b32_e32 v192, v206
	v_mov_b32_e32 v193, v204
	s_mov_b32 m0, s55
	ds_read_b128 v[148:151], v219 offset:32768
	ds_read_b128 v[152:155], v219 offset:33792
	ds_read_b128 v[156:159], v219 offset:34816
	ds_read_b128 v[168:171], v219 offset:35840
	ds_read_b128 v[176:179], v219 offset:36864
	ds_read_b128 v[180:183], v219 offset:37888
	ds_read_b128 v[184:187], v219 offset:38912
	ds_read_b128 v[188:191], v219 offset:39936
	s_nop 0
	global_load_lds_dwordx4 v193, s[50:51]
	s_mov_b32 m0, s56
	s_nop 0
	global_load_lds_dwordx4 v192, s[50:51]
	s_waitcnt vmcnt(8)
	s_waitcnt lgkmcnt(0)
	s_barrier
	s_setprio 1
	s_waitcnt lgkmcnt(0)
	v_mfma_f32_16x16x32_bf16 v[172:175], v[68:71], v[148:151], v[172:175]
	v_mfma_f32_16x16x32_bf16 v[164:167], v[92:95], v[148:151], v[164:167]
	v_mfma_f32_16x16x32_bf16 v[132:135], v[68:71], v[156:159], v[132:135]
	v_mfma_f32_16x16x32_bf16 v[124:127], v[92:95], v[156:159], v[124:127]
	v_mfma_f32_16x16x32_bf16 v[108:111], v[68:71], v[176:179], v[108:111]
	v_mfma_f32_16x16x32_bf16 v[100:103], v[92:95], v[176:179], v[100:103]
	v_mfma_f32_16x16x32_bf16 v[84:87], v[68:71], v[184:187], v[84:87]
	v_mfma_f32_16x16x32_bf16 v[76:79], v[92:95], v[184:187], v[76:79]
	v_mfma_f32_16x16x32_bf16 v[172:175], v[80:83], v[152:155], v[172:175]
	v_mfma_f32_16x16x32_bf16 v[164:167], v[104:107], v[152:155], v[164:167]
	v_mfma_f32_16x16x32_bf16 v[132:135], v[80:83], v[168:171], v[132:135]
	v_mfma_f32_16x16x32_bf16 v[124:127], v[104:107], v[168:171], v[124:127]
	v_mfma_f32_16x16x32_bf16 v[108:111], v[80:83], v[180:183], v[108:111]
	v_mfma_f32_16x16x32_bf16 v[100:103], v[104:107], v[180:183], v[100:103]
	v_mfma_f32_16x16x32_bf16 v[84:87], v[80:83], v[188:191], v[84:87]
	v_mfma_f32_16x16x32_bf16 v[76:79], v[104:107], v[188:191], v[76:79]
	s_setprio 0
	s_setprio 1
	v_mfma_f32_16x16x32_bf16 v[160:163], v[116:119], v[148:151], v[160:163]
	v_mfma_f32_16x16x32_bf16 v[144:147], v[136:139], v[148:151], v[144:147]
	v_mfma_f32_16x16x32_bf16 v[120:123], v[116:119], v[156:159], v[120:123]
	v_mfma_f32_16x16x32_bf16 v[112:115], v[136:139], v[156:159], v[112:115]
	v_mfma_f32_16x16x32_bf16 v[96:99], v[116:119], v[176:179], v[96:99]
	v_mfma_f32_16x16x32_bf16 v[88:91], v[136:139], v[176:179], v[88:91]
	v_mfma_f32_16x16x32_bf16 v[72:75], v[116:119], v[184:187], v[72:75]
	v_mfma_f32_16x16x32_bf16 v[64:67], v[136:139], v[184:187], v[64:67]
	v_mfma_f32_16x16x32_bf16 v[160:163], v[128:131], v[152:155], v[160:163]
	v_mfma_f32_16x16x32_bf16 v[152:155], v[140:143], v[152:155], v[144:147]
	v_mfma_f32_16x16x32_bf16 v[120:123], v[128:131], v[168:171], v[120:123]
	v_mfma_f32_16x16x32_bf16 v[112:115], v[140:143], v[168:171], v[112:115]
	v_mfma_f32_16x16x32_bf16 v[96:99], v[128:131], v[180:183], v[96:99]
	v_mfma_f32_16x16x32_bf16 v[88:91], v[140:143], v[180:183], v[88:91]
	v_mfma_f32_16x16x32_bf16 v[72:75], v[128:131], v[188:191], v[72:75]
	v_mfma_f32_16x16x32_bf16 v[64:67], v[140:143], v[188:191], v[64:67]
	s_setprio 0
	s_barrier
	s_add_u32 s48, s48, 0x80
	s_addc_u32 s49, s49, 0
	s_add_i32 s50, s87, s31
	v_mov_b32_e32 v192, v214
	v_mov_b32_e32 v193, v215
	s_mov_b32 m0, s50
	ds_read_b128 v[144:147], v219 offset:49152
	ds_read_b128 v[148:151], v219 offset:50176
	ds_read_b128 v[156:159], v219 offset:51200
	ds_read_b128 v[168:171], v219 offset:52224
	ds_read_b128 v[176:179], v219 offset:53248
	ds_read_b128 v[180:183], v219 offset:54272
	ds_read_b128 v[184:187], v219 offset:55296
	ds_read_b128 v[188:191], v219 offset:56320
	s_nop 0
	global_load_lds_dwordx4 v192, s[48:49]
	s_add_i32 m0, s50, 0x2000
	v_mov_b32_e32 v192, v214
	global_load_lds_dwordx4 v193, s[48:49]
	s_add_u32 s48, s52, 0x80
	s_addc_u32 s49, s53, 0
	s_add_i32 s50, s88, s31
	v_mov_b32_e32 v193, v215
	s_mov_b32 m0, s50
	s_nop 0
	global_load_lds_dwordx4 v192, s[48:49]
	s_add_i32 m0, s50, 0x2000
	s_add_u32 s12, s12, 0x80
	global_load_lds_dwordx4 v193, s[48:49]
	s_addc_u32 s13, s13, 0
	v_mov_b32_e32 v192, v206
	v_mov_b32_e32 v193, v204
	s_mov_b32 m0, s60
	s_nop 0
	global_load_lds_dwordx4 v193, s[12:13]
	s_mov_b32 m0, s61
	s_nop 0
	global_load_lds_dwordx4 v192, s[12:13]
	s_waitcnt vmcnt(8)
	s_waitcnt lgkmcnt(0)
	s_barrier
	s_setprio 1
	s_waitcnt lgkmcnt(0)
	v_mfma_f32_16x16x32_bf16 v[60:63], v[68:71], v[144:147], v[60:63]
	v_mfma_f32_16x16x32_bf16 v[56:59], v[92:95], v[144:147], v[56:59]
	v_mfma_f32_16x16x32_bf16 v[44:47], v[68:71], v[156:159], v[44:47]
	v_mfma_f32_16x16x32_bf16 v[40:43], v[92:95], v[156:159], v[40:43]
	v_mfma_f32_16x16x32_bf16 v[28:31], v[68:71], v[176:179], v[28:31]
	v_mfma_f32_16x16x32_bf16 v[24:27], v[92:95], v[176:179], v[24:27]
	v_mfma_f32_16x16x32_bf16 v[12:15], v[68:71], v[184:187], v[12:15]
	v_mfma_f32_16x16x32_bf16 v[8:11], v[92:95], v[184:187], v[8:11]
	v_mfma_f32_16x16x32_bf16 v[60:63], v[80:83], v[148:151], v[60:63]
	v_mfma_f32_16x16x32_bf16 v[56:59], v[104:107], v[148:151], v[56:59]
	v_mfma_f32_16x16x32_bf16 v[44:47], v[80:83], v[168:171], v[44:47]
	v_mfma_f32_16x16x32_bf16 v[40:43], v[104:107], v[168:171], v[40:43]
	v_mfma_f32_16x16x32_bf16 v[28:31], v[80:83], v[180:183], v[28:31]
	v_mfma_f32_16x16x32_bf16 v[24:27], v[104:107], v[180:183], v[24:27]
	v_mfma_f32_16x16x32_bf16 v[12:15], v[80:83], v[188:191], v[12:15]
	v_mfma_f32_16x16x32_bf16 v[8:11], v[104:107], v[188:191], v[8:11]
	s_setprio 0
	s_setprio 1
	v_mfma_f32_16x16x32_bf16 v[52:55], v[116:119], v[144:147], v[52:55]
	v_mfma_f32_16x16x32_bf16 v[48:51], v[136:139], v[144:147], v[48:51]
	v_mfma_f32_16x16x32_bf16 v[36:39], v[116:119], v[156:159], v[36:39]
	v_mfma_f32_16x16x32_bf16 v[32:35], v[136:139], v[156:159], v[32:35]
	v_mfma_f32_16x16x32_bf16 v[20:23], v[116:119], v[176:179], v[20:23]
	v_mfma_f32_16x16x32_bf16 v[16:19], v[136:139], v[176:179], v[16:19]
	v_mfma_f32_16x16x32_bf16 v[4:7], v[116:119], v[184:187], v[4:7]
	v_mfma_f32_16x16x32_bf16 v[0:3], v[136:139], v[184:187], v[0:3]
	v_mfma_f32_16x16x32_bf16 v[52:55], v[128:131], v[148:151], v[52:55]
	v_mfma_f32_16x16x32_bf16 v[48:51], v[140:143], v[148:151], v[48:51]
	v_mfma_f32_16x16x32_bf16 v[36:39], v[128:131], v[168:171], v[36:39]
	v_mfma_f32_16x16x32_bf16 v[32:35], v[140:143], v[168:171], v[32:35]
	v_mfma_f32_16x16x32_bf16 v[20:23], v[128:131], v[180:183], v[20:23]
	v_mfma_f32_16x16x32_bf16 v[16:19], v[140:143], v[180:183], v[16:19]
	v_mfma_f32_16x16x32_bf16 v[4:7], v[128:131], v[188:191], v[4:7]
	v_mfma_f32_16x16x32_bf16 v[0:3], v[140:143], v[188:191], v[0:3]
	s_setprio 0
	s_barrier
	s_add_u32 s78, s78, 0x100
	s_addc_u32 s79, s79, 0
	s_add_u32 s80, s80, 0x100
	s_addc_u32 s81, s81, 0
	s_add_u32 s82, s82, 0x100
	s_addc_u32 s83, s83, 0
	s_add_u32 s84, s84, 0x100
	s_addc_u32 s85, s85, 0
	s_cmp_ge_i32 s86, s3
	s_mov_b32 s12, s86
	s_cbranch_scc0 .LBB0_1434
	s_and_b64 vcc, exec, s[28:29]
	s_cbranch_vccz .LBB0_1437
